# code placement: whole instruction stream shifted by 4 bytes (every hot loop head at the opposite byte phase of the baseline's)
# baseline (speedup 1.0000x reference)
_Z10fwd_kernel4Args:
	s_nop 0
	s_load_dwordx2 s[92:93], s[0:1], 0xa0
	s_load_dword s90, s[0:1], 0xb0
	s_load_dwordx8 s[4:11], s[0:1], 0x80
	v_readfirstlane_b32 s3, v0
	s_mov_b32 s96, s2
	s_waitcnt lgkmcnt(0)
	v_writelane_b32 v254, s4, 0
	s_nop 1
	v_writelane_b32 v254, s5, 1
	v_writelane_b32 v254, s6, 2
	v_writelane_b32 v254, s7, 3
	v_writelane_b32 v254, s8, 4
	v_writelane_b32 v254, s9, 5
	v_writelane_b32 v254, s10, 6
	v_writelane_b32 v254, s11, 7
	s_add_u32 s4, s0, 0xb0
	v_writelane_b32 v254, s3, 8
	s_addc_u32 s5, s1, 0
	v_writelane_b32 v254, s4, 9
	s_and_b32 s3, s90, 7
	s_cmp_lg_u32 s3, 0
	v_writelane_b32 v254, s5, 10
	s_cbranch_scc1 .LBB0_2
	s_ashr_i32 s4, s2, 31
	s_lshr_b32 s4, s4, 29
	s_add_i32 s4, s2, s4
	s_ashr_i32 s5, s4, 3
	s_and_b32 s4, s4, -8
	s_ashr_i32 s3, s90, 3
	s_sub_i32 s4, s2, s4
	s_mul_i32 s3, s3, s4
	s_add_i32 s96, s3, s5
